# P2 stage D1: priority raised (s_setprio 2) for the forward-substitution chain waves over the co-resident E-stage waves; stacked on stage B pipelining
# baseline (speedup 1.0000x reference)
.LBB0_407:
	s_andn2_b64 vcc, exec, s[94:95]
	s_cbranch_vccnz .LBB0_443
	v_mov_b32_e32 v1, s9
	s_setprio 2
	ds_read_b128 v[4:7], v1 offset:256
	ds_read_b128 v[8:11], v1 offset:512
	ds_read_b128 v[12:15], v1 offset:768
	ds_read_b128 v[150:153], v1 offset:1024
	ds_read_b128 v[154:157], v1 offset:1280
	ds_read_b128 v[158:161], v1 offset:1296
	ds_read_b128 v[228:231], v1 offset:1536
	ds_read_b128 v[232:235], v1 offset:1552
	ds_read_b128 v[236:239], v1 offset:1792
	ds_read_b128 v[240:243], v1 offset:1808
	ds_read_b128 v[244:247], v1 offset:2048
	v_and_b32_e32 v16, 15, v186
	v_cmp_eq_u32_e32 vcc, 0, v16
	v_bfe_u32 v2, v186, 4, 2
	s_mov_b64 s[70:71], s[96:97]
	v_cndmask_b32_e64 v211, 0, 1.0, vcc
	v_cmp_eq_u32_e32 vcc, 1, v16
	s_waitcnt lgkmcnt(10)
	v_fma_f32 v252, v211, v4, 0
	s_nop 1
	v_cndmask_b32_e64 v248, 0, 1.0, vcc
	v_sub_f32_e32 v212, v248, v252
	ds_read_b128 v[4:7], v1 offset:2064
	v_cmp_eq_u32_e32 vcc, 2, v16
	s_waitcnt lgkmcnt(10)
	v_fma_f32 v252, v211, v8, 0
	v_fma_f32 v253, v9, v212, 0
	v_add_f32_e32 v252, v252, v253
	v_cndmask_b32_e64 v248, 0, 1.0, vcc
	v_sub_f32_e32 v213, v248, v252
	ds_read_b128 v[8:11], v1 offset:2304
	v_cmp_eq_u32_e32 vcc, 3, v16
	s_waitcnt lgkmcnt(10)
	v_fma_f32 v252, v211, v12, 0
	v_fma_f32 v253, v13, v212, 0
	v_fmac_f32_e32 v252, v14, v213
	v_add_f32_e32 v252, v252, v253
	v_cndmask_b32_e64 v248, 0, 1.0, vcc
	v_sub_f32_e32 v17, v248, v252
	ds_read_b128 v[12:15], v1 offset:2320
	v_cmp_eq_u32_e32 vcc, 4, v16
	s_waitcnt lgkmcnt(10)
	v_fma_f32 v252, v211, v150, 0
	v_fma_f32 v253, v151, v212, 0
	v_fmac_f32_e32 v252, v152, v213
	v_fmac_f32_e32 v253, v153, v17
	v_add_f32_e32 v252, v252, v253
	v_cndmask_b32_e64 v248, 0, 1.0, vcc
	v_sub_f32_e32 v214, v248, v252
	ds_read_b128 v[150:153], v1 offset:2336
	v_cmp_eq_u32_e32 vcc, 5, v16
	s_waitcnt lgkmcnt(9)
	v_fma_f32 v252, v211, v154, 0
	v_fma_f32 v253, v155, v212, 0
	v_fmac_f32_e32 v252, v156, v213
	v_fmac_f32_e32 v253, v157, v17
	v_fmac_f32_e32 v252, v158, v214
	v_add_f32_e32 v252, v252, v253
	v_cndmask_b32_e64 v248, 0, 1.0, vcc
	v_sub_f32_e32 v215, v248, v252
	ds_read_b128 v[154:157], v1 offset:2560
	ds_read_b128 v[158:161], v1 offset:2576
	v_cmp_eq_u32_e32 vcc, 6, v16
	s_waitcnt lgkmcnt(9)
	v_fma_f32 v252, v211, v228, 0
	v_fma_f32 v253, v229, v212, 0
	v_fmac_f32_e32 v252, v230, v213
	v_fmac_f32_e32 v253, v231, v17
	v_fmac_f32_e32 v252, v232, v214
	v_fmac_f32_e32 v253, v233, v215
	v_add_f32_e32 v252, v252, v253
	v_cndmask_b32_e64 v248, 0, 1.0, vcc
	v_sub_f32_e32 v217, v248, v252
	ds_read_b128 v[228:231], v1 offset:2592
	ds_read_b128 v[232:235], v1 offset:2816
	v_cmp_eq_u32_e32 vcc, 7, v16
	s_waitcnt lgkmcnt(9)
	v_fma_f32 v252, v211, v236, 0
	v_fma_f32 v253, v237, v212, 0
	v_fmac_f32_e32 v252, v238, v213
	v_fmac_f32_e32 v253, v239, v17
	v_fmac_f32_e32 v252, v240, v214
	v_fmac_f32_e32 v253, v241, v215
	v_fmac_f32_e32 v252, v242, v217
	v_add_f32_e32 v252, v252, v253
	v_cndmask_b32_e64 v248, 0, 1.0, vcc
	v_sub_f32_e32 v216, v248, v252
	ds_read_b128 v[236:239], v1 offset:2832
	ds_read_b128 v[240:243], v1 offset:2848
	v_cmp_eq_u32_e32 vcc, 8, v16
	s_waitcnt lgkmcnt(9)
	v_fma_f32 v252, v211, v244, 0
	v_fma_f32 v253, v245, v212, 0
	v_fmac_f32_e32 v252, v246, v213
	v_fmac_f32_e32 v253, v247, v17
	v_fmac_f32_e32 v252, v4, v214
	v_fmac_f32_e32 v253, v5, v215
	v_fmac_f32_e32 v252, v6, v217
	v_fmac_f32_e32 v253, v7, v216
	v_add_f32_e32 v252, v252, v253
	v_cndmask_b32_e64 v248, 0, 1.0, vcc
	v_sub_f32_e32 v219, v248, v252
	v_cmp_eq_u32_e32 vcc, 9, v16
	s_waitcnt lgkmcnt(6)
	v_fma_f32 v252, v211, v8, 0
	v_fma_f32 v253, v9, v212, 0
	v_fmac_f32_e32 v252, v10, v213
	v_fmac_f32_e32 v253, v11, v17
	v_fmac_f32_e32 v252, v12, v214
	v_fmac_f32_e32 v253, v13, v215
	v_fmac_f32_e32 v252, v14, v217
	v_fmac_f32_e32 v253, v15, v216
	v_fmac_f32_e32 v252, v150, v219
	v_add_f32_e32 v252, v252, v253
	v_cndmask_b32_e64 v248, 0, 1.0, vcc
	v_sub_f32_e32 v220, v248, v252
	v_cmp_eq_u32_e32 vcc, 10, v16
	s_waitcnt lgkmcnt(3)
	v_fma_f32 v252, v211, v154, 0
	v_fma_f32 v253, v155, v212, 0
	v_fmac_f32_e32 v252, v156, v213
	v_fmac_f32_e32 v253, v157, v17
	v_fmac_f32_e32 v252, v158, v214
	v_fmac_f32_e32 v253, v159, v215
	v_fmac_f32_e32 v252, v160, v217
	v_fmac_f32_e32 v253, v161, v216
	v_fmac_f32_e32 v252, v228, v219
	v_fmac_f32_e32 v253, v229, v220
	v_add_f32_e32 v252, v252, v253
	v_cndmask_b32_e64 v248, 0, 1.0, vcc
	v_sub_f32_e32 v221, v248, v252
	v_cmp_eq_u32_e32 vcc, 11, v16
	s_waitcnt lgkmcnt(0)
	v_fma_f32 v252, v211, v232, 0
	v_fma_f32 v253, v233, v212, 0
	v_fmac_f32_e32 v252, v234, v213
	v_fmac_f32_e32 v253, v235, v17
	v_fmac_f32_e32 v252, v236, v214
	v_fmac_f32_e32 v253, v237, v215
	v_fmac_f32_e32 v252, v238, v217
	v_fmac_f32_e32 v253, v239, v216
	v_fmac_f32_e32 v252, v240, v219
	v_fmac_f32_e32 v253, v241, v220
	v_fmac_f32_e32 v252, v242, v221
	v_add_f32_e32 v252, v252, v253
	v_cndmask_b32_e64 v248, 0, 1.0, vcc
	v_sub_f32_e32 v222, v248, v252
	s_setprio 0
	ds_read_b128 v[4:7], v1 offset:3072
	ds_read_b128 v[8:11], v1 offset:3088
	ds_read_b128 v[12:15], v1 offset:3104
	ds_read_b128 v[182:185], v1 offset:3328
	ds_read_b128 v[178:181], v1 offset:3344
	ds_read_b128 v[174:177], v1 offset:3360
	ds_read_b128 v[170:173], v1 offset:3376
	s_waitcnt lgkmcnt(6)
	v_fma_f32 v4, v211, v4, 0
	v_fma_f32 v5, v212, v5, 0
	v_fmac_f32_e32 v4, v213, v6
	v_fmac_f32_e32 v5, v17, v7
	s_waitcnt lgkmcnt(5)
	v_fmac_f32_e32 v4, v214, v8
	v_fmac_f32_e32 v5, v215, v9
	v_fmac_f32_e32 v4, v10, v217
	v_fmac_f32_e32 v5, v11, v216
	s_waitcnt lgkmcnt(4)
	v_fmac_f32_e32 v4, v12, v219
	v_fmac_f32_e32 v5, v13, v220
	v_fmac_f32_e32 v4, v14, v221
	v_fmac_f32_e32 v5, v15, v222
	v_cmp_eq_u32_e32 vcc, 12, v16
	v_add_f32_e32 v4, v4, v5
	s_nop 0
	v_cndmask_b32_e64 v6, 0, 1.0, vcc
	s_waitcnt lgkmcnt(0)
	v_sub_f32_e32 v171, v6, v4
	ds_read_b128 v[166:169], v1 offset:3584
	ds_read_b128 v[162:165], v1 offset:3600
	ds_read_b128 v[158:161], v1 offset:3616
	ds_read_b128 v[154:157], v1 offset:3632
	ds_read_b128 v[150:153], v1 offset:3840
	ds_read_b128 v[12:15], v1 offset:3856
	ds_read_b128 v[8:11], v1 offset:3872
	ds_read_b128 v[4:7], v1 offset:3888
	v_cmp_lt_i32_e32 vcc, 1, v2
	s_and_saveexec_b64 s[94:95], vcc
	s_xor_b64 s[94:95], exec, s[94:95]
	s_cbranch_execz .LBB0_412
	v_cmp_lt_i32_e32 vcc, 2, v2
	s_and_saveexec_b64 s[96:97], vcc
	s_xor_b64 s[96:97], exec, s[96:97]
	s_or_saveexec_b64 s[96:97], s[96:97]
	v_mov_b32_e32 v223, v171
	s_xor_b64 exec, exec, s[96:97]
	v_mov_b32_e32 v223, v219
	s_or_b64 exec, exec, s[96:97]
